# baseline (speedup 1.0000x reference)
.LBB1_68:
	v_mov_b32_e32 v2, v0
	s_bfe_u32 s21, s8, 0x80010
	s_lshl_b32 s13, s21, 7
	v_lshrrev_b32_e32 v3, 2, v2
	v_and_b32_e32 v3, 0xffffe0, v3
	v_add_u32_e32 v3, s13, v3
	v_lshrrev_b32_e32 v4, 3, v2
	v_and_or_b32 v3, v4, 7, v3
	s_movk_i32 s6, 0x300
	v_mul_lo_u32 v3, v3, s6
	v_lshlrev_b32_e32 v2, 2, v2
	v_and_or_b32 v2, v2, 28, v3
	v_lshlrev_b32_e32 v2, 2, v2
	v_mov_b32_e32 v3, 0
	v_lshl_add_u64 v[4:5], s[2:3], 0, v[2:3]
	global_load_dwordx4 v[26:29], v2, s[2:3] nt
	global_load_dwordx4 v[18:21], v2, s[2:3] offset:128 nt
	global_load_dwordx4 v[114:117], v2, s[2:3] offset:256 nt
	global_load_dwordx4 v[118:121], v2, s[2:3] offset:384 nt
	s_movk_i32 s2, 0x6000
	v_add_co_u32_e32 v2, vcc, s2, v4
	s_mov_b32 s2, 0xc000
	s_nop 0
	v_addc_co_u32_e32 v3, vcc, 0, v5, vcc
	global_load_dwordx4 v[30:33], v[2:3], off nt
	global_load_dwordx4 v[14:17], v[2:3], off offset:128 nt
	global_load_dwordx4 v[122:125], v[2:3], off offset:256 nt
	global_load_dwordx4 v[126:129], v[2:3], off offset:384 nt
	v_add_co_u32_e32 v2, vcc, s2, v4
	s_nop 1
	v_addc_co_u32_e32 v3, vcc, 0, v5, vcc
	v_add_co_u32_e32 v36, vcc, 0x12000, v4
	global_load_dwordx4 v[22:25], v[2:3], off nt
	global_load_dwordx4 v[6:9], v[2:3], off offset:128 nt
	global_load_dwordx4 v[130:133], v[2:3], off offset:256 nt
	global_load_dwordx4 v[134:137], v[2:3], off offset:384 nt
	v_addc_co_u32_e32 v37, vcc, 0, v5, vcc
	global_load_dwordx4 v[10:13], v[36:37], off nt
	global_load_dwordx4 v[138:141], v[36:37], off offset:256 nt
	global_load_dwordx4 v[142:145], v[36:37], off offset:384 nt
	global_load_dwordx4 v[2:5], v[36:37], off offset:128 nt
	v_cmp_gt_u32_e32 vcc, 64, v0
	s_and_b32 s12, s8, 0xffff
	s_and_saveexec_b64 s[6:7], vcc
	s_cbranch_execz .LBB1_78
	s_cmp_eq_u32 s9, 8
	s_cselect_b64 vcc, -1, 0
	s_add_i32 s2, s12, 0xffffe800
	v_mov_b32_e32 v37, 0x24000
	v_add_u32_e32 v35, s2, v34
	v_add_u32_e32 v38, 64, v35
	v_cndmask_b32_e32 v36, 0, v35, vcc
	v_lshl_add_u32 v37, v34, 2, v37
	v_cndmask_b32_e32 v38, 0, v38, vcc
	ds_write2st64_b32 v37, v36, v38 offset1:1
	v_add_u32_e32 v36, 0x80, v35
	v_add_u32_e32 v35, 0xc0, v35
	v_cndmask_b32_e32 v36, 0, v36, vcc
	v_cndmask_b32_e32 v35, 0, v35, vcc
	s_andn2_b64 vcc, exec, s[0:1]
	ds_write2st64_b32 v37, v36, v35 offset0:2 offset1:3
	s_cbranch_vccnz .LBB1_78
	v_mov_b32_e32 v35, 0x20000
	v_lshl_add_u32 v44, v34, 3, v35
	ds_read2st64_b64 v[36:39], v44 offset1:1
	ds_read2st64_b64 v[40:43], v44 offset0:2 offset1:3
	v_mov_b32_e32 v61, 0x100
	v_mov_b32_e32 v69, 0x1000
	v_mov_b32_e32 v77, 0x10000
	s_waitcnt lgkmcnt(1)
	v_cmp_eq_u32_e64 s[2:3], s9, v38
	v_cmp_eq_u32_e32 vcc, s9, v36
	v_cmp_eq_u32_e64 s[0:1], s9, v37
	v_cndmask_b32_e64 v45, 0, 2, s[2:3]
	v_cmp_eq_u32_e64 s[2:3], s9, v39
	ds_read2st64_b64 v[36:39], v44 offset0:4 offset1:5
	v_mov_b32_e32 v84, 0x100000
	v_cndmask_b32_e64 v46, 0, 2, s[2:3]
	s_waitcnt lgkmcnt(1)
	v_cmp_eq_u32_e64 s[2:3], s9, v40
	v_mov_b32_e32 v92, 0x1000000
	v_bfrev_b32_e32 v100, 8
	v_cndmask_b32_e64 v47, 0, 4, s[2:3]
	v_cmp_eq_u32_e64 s[2:3], s9, v41
	s_or_b64 s[0:1], s[0:1], vcc
	s_cmp_lt_u32 s8, 0x1000000
	v_cndmask_b32_e64 v48, 0, 4, s[2:3]
	v_cmp_eq_u32_e64 s[2:3], s9, v42
	s_nop 1
	v_cndmask_b32_e64 v49, 0, 8, s[2:3]
	v_cmp_eq_u32_e64 s[2:3], s9, v43
	ds_read2st64_b64 v[40:43], v44 offset0:6 offset1:7
	s_nop 0
	v_cndmask_b32_e64 v52, 0, 8, s[2:3]
	s_waitcnt lgkmcnt(1)
	v_cmp_eq_u32_e64 s[2:3], s9, v36
	s_nop 1
	v_cndmask_b32_e64 v53, 0, 16, s[2:3]
	v_cmp_eq_u32_e64 s[2:3], s9, v37
	s_nop 1
	v_cndmask_b32_e64 v54, 0, 16, s[2:3]
	v_cmp_eq_u32_e64 s[2:3], s9, v38
	s_nop 1
	v_cndmask_b32_e64 v55, 0, 32, s[2:3]
	v_cmp_eq_u32_e64 s[2:3], s9, v39
	ds_read2st64_b64 v[36:39], v44 offset0:8 offset1:9
	s_nop 0
	v_cndmask_b32_e64 v56, 0, 32, s[2:3]
	s_waitcnt lgkmcnt(1)
	v_cmp_eq_u32_e64 s[2:3], s9, v40
	v_mov_b32_e32 v40, 0x80
	s_nop 0
	v_cndmask_b32_e64 v57, 0, 64, s[2:3]
	v_cmp_eq_u32_e64 s[2:3], s9, v41
	s_nop 1
	v_cndmask_b32_e64 v58, 0, 64, s[2:3]
	v_cmp_eq_u32_e64 s[2:3], s9, v42
	s_nop 1
	v_cndmask_b32_e64 v59, 0, v40, s[2:3]
	v_cmp_eq_u32_e64 s[2:3], s9, v43
	s_nop 1
	v_cndmask_b32_e64 v60, 0, v40, s[2:3]
	ds_read2st64_b64 v[40:43], v44 offset0:10 offset1:11
	s_waitcnt lgkmcnt(1)
	v_cmp_eq_u32_e64 s[2:3], s9, v36
	v_mov_b32_e32 v36, 0x200
	s_nop 0
	v_cndmask_b32_e64 v62, 0, v61, s[2:3]
	v_cmp_eq_u32_e64 s[2:3], s9, v37
	s_nop 1
	v_cndmask_b32_e64 v61, 0, v61, s[2:3]
	v_cmp_eq_u32_e64 s[2:3], s9, v38
	s_nop 1
	v_cndmask_b32_e64 v63, 0, v36, s[2:3]
	v_cmp_eq_u32_e64 s[2:3], s9, v39
	s_nop 1
	v_cndmask_b32_e64 v64, 0, v36, s[2:3]
	v_mov_b32_e32 v36, 0x400
	s_waitcnt lgkmcnt(0)
	v_cmp_eq_u32_e64 s[2:3], s9, v40
	v_mov_b32_e32 v40, 0x800
	s_nop 0
	v_cndmask_b32_e64 v65, 0, v36, s[2:3]
	v_cmp_eq_u32_e64 s[2:3], s9, v41
	s_nop 1
	v_cndmask_b32_e64 v66, 0, v36, s[2:3]
	ds_read2st64_b64 v[36:39], v44 offset0:12 offset1:13
	v_cmp_eq_u32_e64 s[2:3], s9, v42
	s_nop 1
	v_cndmask_b32_e64 v67, 0, v40, s[2:3]
	v_cmp_eq_u32_e64 s[2:3], s9, v43
	s_nop 1
	v_cndmask_b32_e64 v68, 0, v40, s[2:3]
	ds_read2st64_b64 v[40:43], v44 offset0:14 offset1:15
	s_waitcnt lgkmcnt(1)
	v_cmp_eq_u32_e64 s[2:3], s9, v36
	v_mov_b32_e32 v36, 0x2000
	s_nop 0
	v_cndmask_b32_e64 v70, 0, v69, s[2:3]
	v_cmp_eq_u32_e64 s[2:3], s9, v37
	s_nop 1
	v_cndmask_b32_e64 v69, 0, v69, s[2:3]
	v_cmp_eq_u32_e64 s[2:3], s9, v38
	s_nop 1
	v_cndmask_b32_e64 v71, 0, v36, s[2:3]
	v_cmp_eq_u32_e64 s[2:3], s9, v39
	s_nop 1
	v_cndmask_b32_e64 v72, 0, v36, s[2:3]
	v_mov_b32_e32 v36, 0x4000
	s_waitcnt lgkmcnt(0)
	v_cmp_eq_u32_e64 s[2:3], s9, v40
	v_mov_b32_e32 v40, 0x8000
	s_nop 0
	v_cndmask_b32_e64 v73, 0, v36, s[2:3]
	v_cmp_eq_u32_e64 s[2:3], s9, v41
	s_nop 1
	v_cndmask_b32_e64 v74, 0, v36, s[2:3]
	ds_read2st64_b64 v[36:39], v44 offset0:16 offset1:17
	v_cmp_eq_u32_e64 s[2:3], s9, v42
	s_nop 1
	v_cndmask_b32_e64 v75, 0, v40, s[2:3]
	v_cmp_eq_u32_e64 s[2:3], s9, v43
	s_nop 1
	v_cndmask_b32_e64 v76, 0, v40, s[2:3]
	ds_read2st64_b64 v[40:43], v44 offset0:18 offset1:19
	s_waitcnt lgkmcnt(1)
	v_cmp_eq_u32_e64 s[2:3], s9, v36
	v_mov_b32_e32 v36, 0x40000
	s_nop 0
	v_cndmask_b32_e64 v78, 0, v77, s[2:3]
	v_cmp_eq_u32_e64 s[2:3], s9, v37
	s_nop 1
	v_cndmask_b32_e64 v77, 0, v77, s[2:3]
	v_cmp_eq_u32_e64 s[2:3], s9, v38
	s_nop 1
	v_cndmask_b32_e64 v79, 0, v35, s[2:3]
	v_cmp_eq_u32_e64 s[2:3], s9, v39
	s_nop 1
	v_cndmask_b32_e64 v35, 0, v35, s[2:3]
	s_waitcnt lgkmcnt(0)
	v_cmp_eq_u32_e64 s[2:3], s9, v40
	v_mov_b32_e32 v40, 0x80000
	s_nop 0
	v_cndmask_b32_e64 v80, 0, v36, s[2:3]
	v_cmp_eq_u32_e64 s[2:3], s9, v41
	s_nop 1
	v_cndmask_b32_e64 v81, 0, v36, s[2:3]
	ds_read2st64_b64 v[36:39], v44 offset0:20 offset1:21
	v_cmp_eq_u32_e64 s[2:3], s9, v42
	s_nop 1
	v_cndmask_b32_e64 v82, 0, v40, s[2:3]
	v_cmp_eq_u32_e64 s[2:3], s9, v43
	s_nop 1
	v_cndmask_b32_e64 v83, 0, v40, s[2:3]
	ds_read2st64_b64 v[40:43], v44 offset0:22 offset1:23
	s_waitcnt lgkmcnt(1)
	v_cmp_eq_u32_e64 s[2:3], s9, v36
	v_mov_b32_e32 v36, 0x200000
	s_nop 0
	v_cndmask_b32_e64 v85, 0, v84, s[2:3]
	v_cmp_eq_u32_e64 s[2:3], s9, v37
	s_nop 1
	v_cndmask_b32_e64 v84, 0, v84, s[2:3]
	v_cmp_eq_u32_e64 s[2:3], s9, v38
	s_nop 1
	v_cndmask_b32_e64 v86, 0, v36, s[2:3]
	v_cmp_eq_u32_e64 s[2:3], s9, v39
	s_nop 1
	v_cndmask_b32_e64 v87, 0, v36, s[2:3]
	v_mov_b32_e32 v36, 0x400000
	s_waitcnt lgkmcnt(0)
	v_cmp_eq_u32_e64 s[2:3], s9, v40
	v_mov_b32_e32 v40, 0x800000
	s_nop 0
	v_cndmask_b32_e64 v88, 0, v36, s[2:3]
	v_cmp_eq_u32_e64 s[2:3], s9, v41
	s_nop 1
	v_cndmask_b32_e64 v89, 0, v36, s[2:3]
	ds_read2st64_b64 v[36:39], v44 offset0:24 offset1:25
	v_cmp_eq_u32_e64 s[2:3], s9, v42
	s_nop 1
	v_cndmask_b32_e64 v90, 0, v40, s[2:3]
	v_cmp_eq_u32_e64 s[2:3], s9, v43
	s_nop 1
	v_cndmask_b32_e64 v91, 0, v40, s[2:3]
	ds_read2st64_b64 v[40:43], v44 offset0:26 offset1:27
	s_waitcnt lgkmcnt(1)
	v_cmp_eq_u32_e64 s[2:3], s9, v36
	v_bfrev_b32_e32 v36, 64
	s_nop 0
	v_cndmask_b32_e64 v93, 0, v92, s[2:3]
	v_cmp_eq_u32_e64 s[2:3], s9, v37
	s_nop 1
	v_cndmask_b32_e64 v92, 0, v92, s[2:3]
	v_cmp_eq_u32_e64 s[2:3], s9, v38
	s_nop 1
	v_cndmask_b32_e64 v94, 0, v36, s[2:3]
	v_cmp_eq_u32_e64 s[2:3], s9, v39
	s_nop 1
	v_cndmask_b32_e64 v95, 0, v36, s[2:3]
	v_bfrev_b32_e32 v36, 32
	s_waitcnt lgkmcnt(0)
	v_cmp_eq_u32_e64 s[2:3], s9, v40
	v_bfrev_b32_e32 v40, 16
	s_nop 0
	v_cndmask_b32_e64 v96, 0, v36, s[2:3]
	v_cmp_eq_u32_e64 s[2:3], s9, v41
	s_nop 1
	v_cndmask_b32_e64 v97, 0, v36, s[2:3]
	ds_read2st64_b64 v[36:39], v44 offset0:28 offset1:29
	v_cmp_eq_u32_e64 s[2:3], s9, v42
	s_nop 1
	v_cndmask_b32_e64 v98, 0, v40, s[2:3]
	v_cmp_eq_u32_e64 s[2:3], s9, v43
	s_nop 1
	v_cndmask_b32_e64 v99, 0, v40, s[2:3]
	ds_read2st64_b64 v[40:43], v44 offset0:30 offset1:31
	s_waitcnt lgkmcnt(1)
	v_cmp_eq_u32_e64 s[2:3], s9, v36
	v_bfrev_b32_e32 v44, 4
	s_nop 0
	v_cndmask_b32_e64 v36, 0, v100, s[2:3]
	v_cmp_eq_u32_e64 s[2:3], s9, v37
	s_nop 1
	v_cndmask_b32_e64 v37, 0, v100, s[2:3]
	v_cmp_eq_u32_e64 s[2:3], s9, v38
	s_nop 1
	v_cndmask_b32_e64 v38, 0, v44, s[2:3]
	v_cmp_eq_u32_e64 s[2:3], s9, v39
	s_nop 1
	v_cndmask_b32_e64 v39, 0, v44, s[2:3]
	s_waitcnt lgkmcnt(0)
	v_cmp_eq_u32_e64 s[2:3], s9, v40
	v_bfrev_b32_e32 v44, 1
	s_nop 0
	v_cndmask_b32_e64 v40, 0, 2.0, s[2:3]
	v_cmp_eq_u32_e64 s[2:3], s9, v41
	s_nop 1
	v_cndmask_b32_e64 v41, 0, 2.0, s[2:3]
	v_cmp_eq_u32_e64 s[2:3], s9, v42
	s_nop 1
	v_cndmask_b32_e64 v42, 0, v44, s[2:3]
	v_cmp_eq_u32_e64 s[2:3], s9, v43
	s_nop 1
	v_cndmask_b32_e64 v43, 0, v44, s[2:3]
	v_cndmask_b32_e64 v44, 0, 1, s[0:1]
	v_or3_b32 v44, v45, v44, v46
	v_or3_b32 v44, v44, v47, v48
	v_or3_b32 v44, v44, v49, v52
	v_or3_b32 v44, v44, v53, v54
	v_or3_b32 v44, v44, v55, v56
	v_or3_b32 v44, v44, v57, v58
	v_or3_b32 v44, v44, v59, v60
	v_or3_b32 v44, v44, v62, v61
	v_or3_b32 v44, v44, v63, v64
	v_or3_b32 v44, v44, v65, v66
	v_or3_b32 v44, v44, v67, v68
	v_or3_b32 v44, v44, v70, v69
	v_or3_b32 v44, v44, v71, v72
	v_or3_b32 v44, v44, v73, v74
	v_or3_b32 v44, v44, v75, v76
	v_or3_b32 v44, v44, v78, v77
	v_or3_b32 v35, v44, v79, v35
	v_or3_b32 v35, v35, v80, v81
	v_or3_b32 v35, v35, v82, v83
	v_or3_b32 v35, v35, v85, v84
	v_or3_b32 v35, v35, v86, v87
	v_or3_b32 v35, v35, v88, v89
	v_or3_b32 v35, v35, v90, v91
	v_or3_b32 v35, v35, v93, v92
	v_or3_b32 v35, v35, v94, v95
	v_or3_b32 v35, v35, v96, v97
	v_or3_b32 v35, v35, v98, v99
	v_or3_b32 v35, v35, v36, v37
	v_or3_b32 v35, v35, v38, v39
	v_add_u32_e32 v37, -1, v50
	v_or3_b32 v35, v35, v40, v41
	v_cmp_lt_i32_e32 vcc, v37, v51
	v_or3_b32 v35, v35, v42, v43
	v_bcnt_u32_b32 v36, v35, 0
	v_cndmask_b32_e32 v37, v37, v50, vcc
	v_lshlrev_b32_e32 v37, 2, v37
	ds_bpermute_b32 v37, v37, v36
	v_cmp_lt_i32_e32 vcc, 0, v34
	v_add_u32_e32 v38, -2, v50
	v_mov_b32_e32 v39, 0
	s_waitcnt lgkmcnt(0)
	v_cndmask_b32_e32 v37, 0, v37, vcc
	v_cmp_lt_i32_e32 vcc, v38, v51
	v_bcnt_u32_b32 v37, v35, v37
	s_nop 0
	v_cndmask_b32_e32 v38, v38, v50, vcc
	v_lshlrev_b32_e32 v38, 2, v38
	ds_bpermute_b32 v38, v38, v37
	v_cmp_lt_i32_e32 vcc, 1, v34
	s_waitcnt lgkmcnt(0)
	s_nop 0
	v_cndmask_b32_e32 v38, 0, v38, vcc
	v_add_u32_e32 v37, v38, v37
	v_add_u32_e32 v38, -4, v50
	v_cmp_lt_i32_e32 vcc, v38, v51
	s_nop 1
	v_cndmask_b32_e32 v38, v38, v50, vcc
	v_lshlrev_b32_e32 v38, 2, v38
	ds_bpermute_b32 v38, v38, v37
	v_cmp_lt_i32_e32 vcc, 3, v34
	s_waitcnt lgkmcnt(0)
	s_nop 0
	v_cndmask_b32_e32 v38, 0, v38, vcc
	v_add_u32_e32 v37, v38, v37
	v_add_u32_e32 v38, -8, v50
	v_cmp_lt_i32_e32 vcc, v38, v51
	s_nop 1
	v_cndmask_b32_e32 v38, v38, v50, vcc
	v_lshlrev_b32_e32 v38, 2, v38
	ds_bpermute_b32 v38, v38, v37
	v_cmp_lt_i32_e32 vcc, 7, v34
	s_waitcnt lgkmcnt(0)
	s_nop 0
	v_cndmask_b32_e32 v38, 0, v38, vcc
	v_add_u32_e32 v37, v38, v37
	v_add_u32_e32 v38, -16, v50
	v_cmp_lt_i32_e32 vcc, v38, v51
	s_nop 1
	v_cndmask_b32_e32 v38, v38, v50, vcc
	v_lshlrev_b32_e32 v38, 2, v38
	ds_bpermute_b32 v38, v38, v37
	v_cmp_lt_i32_e32 vcc, 15, v34
	s_waitcnt lgkmcnt(0)
	s_nop 0
	v_cndmask_b32_e32 v38, 0, v38, vcc
	v_add_u32_e32 v37, v38, v37
	v_subrev_u32_e32 v38, 32, v50
	v_cmp_lt_i32_e32 vcc, v38, v51
	s_nop 1
	v_cndmask_b32_e32 v38, v38, v50, vcc
	v_lshlrev_b32_e32 v38, 2, v38
	ds_bpermute_b32 v38, v38, v37
	s_cbranch_scc1 .LBB1_73
	s_mov_b32 s0, 0x24800
	v_mov_b32_e32 v39, 0

.LBB1_82:
	v_mov_b32_e32 v52, v0
	v_mov_b32_e32 v36, v0
	s_movk_i32 s0, 0xff80
	v_lshrrev_b32_e32 v34, 1, v36
	v_and_b32_e32 v34, 28, v34
	v_lshlrev_b32_e32 v35, 1, v36
	v_and_or_b32 v34, v35, s0, v34
	v_add_u32_e32 v37, 0x24000, v34
	ds_read2_b32 v[34:35], v37 offset1:8
	v_lshlrev_b32_e32 v36, 3, v36
	s_movk_i32 s22, 0x300
	v_and_b32_e32 v38, 56, v36
	ds_read2_b32 v[36:37], v37 offset0:16 offset1:24
	s_waitcnt lgkmcnt(1)
	v_mul_lo_u32 v34, v34, s22
	v_or_b32_e32 v34, v34, v38
	v_lshlrev_b32_e32 v198, 1, v34
	v_mul_lo_u32 v34, v35, s22
	v_or_b32_e32 v34, v34, v38
	v_lshlrev_b32_e32 v199, 1, v34
	s_waitcnt lgkmcnt(0)
	v_mul_lo_u32 v34, v36, s22
	v_or_b32_e32 v34, v34, v38
	v_lshlrev_b32_e32 v200, 1, v34
	v_mul_lo_u32 v34, v37, s22
	v_or_b32_e32 v34, v34, v38
	v_lshlrev_b32_e32 v201, 1, v34
	v_mov_b32_e32 v34, v198
	v_mov_b32_e32 v38, v199
	global_load_dwordx4 v[34:37], v34, s[52:53]
	v_mov_b32_e32 v42, v200
	global_load_dwordx4 v[38:41], v38, s[52:53]
	v_mov_b32_e32 v46, v201
	global_load_dwordx4 v[42:45], v42, s[52:53]
	global_load_dwordx4 v[46:49], v46, s[52:53]
	global_load_dwordx4 v[146:149], v198, s[52:53] offset:128
	global_load_dwordx4 v[150:153], v199, s[52:53] offset:128
	global_load_dwordx4 v[154:157], v200, s[52:53] offset:128
	global_load_dwordx4 v[158:161], v201, s[52:53] offset:128
	v_lshrrev_b32_e32 v53, 2, v52
	v_and_b32_e32 v53, 0xffffe0, v53
	v_add_u32_e32 v53, s13, v53
	v_lshrrev_b32_e32 v54, 3, v52
	v_and_or_b32 v53, v54, 7, v53
	v_mul_lo_u32 v53, v53, s22
	v_lshlrev_b32_e32 v52, 2, v52
	v_and_or_b32 v52, v52, 28, v53
	v_mov_b32_e32 v53, v0
	s_movk_i32 s0, 0x400
	v_lshlrev_b32_e32 v57, 4, v53
	v_lshlrev_b32_e32 v54, 8, v53
	v_lshlrev_b32_e32 v55, 3, v53
	v_and_b32_e32 v57, 48, v57
	v_lshlrev_b32_e32 v53, 6, v53
	v_and_b32_e32 v56, 0x1c0, v55
	v_and_or_b32 v54, v54, s0, v57
	v_and_b32_e32 v53, 0xfffff000, v53
	v_or3_b32 v57, v54, v56, v53
	s_waitcnt vmcnt(7)
	ds_write_b128 v57, v[34:37]
	v_bitop3_b32 v34, v54, 32, v56 bitop3:0x36
	v_or_b32_e32 v34, v53, v34
	s_waitcnt vmcnt(6)
	ds_write_b128 v34, v[38:41] offset:512
	s_waitcnt vmcnt(5)
	ds_write_b128 v57, v[42:45] offset:2048
	s_waitcnt vmcnt(4)
	ds_write_b128 v34, v[46:49] offset:2560
	v_and_b32_e32 v34, 0x1f8, v55
	v_cvt_pk_f16_f32 v29, v28, v29
	v_cvt_pk_f16_f32 v28, v26, v27
	v_or_b32_e32 v26, v34, v53
	v_cvt_pk_f16_f32 v21, v20, v21
	v_cvt_pk_f16_f32 v20, v18, v19
	ds_write2st64_b64 v26, v[28:29], v[20:21] offset0:64 offset1:66
	v_mov_b32_e32 v20, 0x1f8
	v_cvt_pk_f16_f32 v17, v16, v17
	v_cvt_pk_f16_f32 v16, v14, v15
	v_cvt_pk_f16_f32 v15, v24, v25
	v_cvt_pk_f16_f32 v14, v22, v23
	v_bitop3_b32 v20, v55, 32, v20 bitop3:0x6c
	ds_write_b64 v26, v[14:15] offset:34816
	v_or_b32_e32 v14, 0xc00, v53
	v_cvt_pk_f16_f32 v19, v32, v33
	v_cvt_pk_f16_f32 v18, v30, v31
	v_or_b32_e32 v21, v20, v53
	v_cvt_pk_f16_f32 v9, v8, v9
	v_cvt_pk_f16_f32 v8, v6, v7
	v_or_b32_e32 v6, v34, v14
	s_movk_i32 s0, 0xf800
	ds_write2st64_b64 v21, v[18:19], v[16:17] offset0:65 offset1:67
	ds_write_b64 v6, v[8:9] offset:32768
	v_cvt_pk_f16_f32 v7, v12, v13
	v_cvt_pk_f16_f32 v6, v10, v11
	v_and_or_b32 v8, v14, s0, v20
	v_cvt_pk_f16_f32 v5, v4, v5
	v_cvt_pk_f16_f32 v4, v2, v3
	v_or_b32_e32 v2, v20, v14
	ds_write_b64 v8, v[6:7] offset:33280
	ds_write_b64 v2, v[4:5] offset:33280
	v_lshlrev_b32_e32 v202, 2, v52
	v_mov_b32_e32 v194, v202
	v_mov_b32_e32 v195, 0
	s_movk_i32 s23, 0x6000
	s_mov_b32 s24, 0xc000
	s_mov_b32 s25, 0x12000
	s_waitcnt vmcnt(0)
	v_mov_b32_e32 v2, v146
	v_mov_b32_e32 v3, v147
	v_mov_b32_e32 v4, v148
	v_mov_b32_e32 v5, v149
	v_mov_b32_e32 v6, v150
	v_mov_b32_e32 v7, v151
	v_mov_b32_e32 v8, v152
	v_mov_b32_e32 v9, v153
	v_mov_b32_e32 v10, v154
	v_mov_b32_e32 v11, v155
	v_mov_b32_e32 v12, v156
	v_mov_b32_e32 v13, v157
	v_mov_b32_e32 v14, v158
	v_mov_b32_e32 v15, v159
	v_mov_b32_e32 v16, v160
	v_mov_b32_e32 v17, v161
	v_mov_b32_e32 v22, v114
	v_mov_b32_e32 v23, v115
	v_mov_b32_e32 v24, v116
	v_mov_b32_e32 v25, v117
	v_mov_b32_e32 v18, v118
	v_mov_b32_e32 v19, v119
	v_mov_b32_e32 v20, v120
	v_mov_b32_e32 v21, v121
	v_mov_b32_e32 v30, v122
	v_mov_b32_e32 v31, v123
	v_mov_b32_e32 v32, v124
	v_mov_b32_e32 v33, v125
	v_mov_b32_e32 v26, v126
	v_mov_b32_e32 v27, v127
	v_mov_b32_e32 v28, v128
	v_mov_b32_e32 v29, v129
	v_mov_b32_e32 v38, v130
	v_mov_b32_e32 v39, v131
	v_mov_b32_e32 v40, v132
	v_mov_b32_e32 v41, v133
	v_mov_b32_e32 v34, v134
	v_mov_b32_e32 v35, v135
	v_mov_b32_e32 v36, v136
	v_mov_b32_e32 v37, v137
	v_mov_b32_e32 v46, v138
	v_mov_b32_e32 v47, v139
	v_mov_b32_e32 v48, v140
	v_mov_b32_e32 v49, v141
	v_mov_b32_e32 v42, v142
	v_mov_b32_e32 v43, v143
	v_mov_b32_e32 v44, v144
	v_mov_b32_e32 v45, v145
	s_movk_i32 s26, 0x1f8
	s_mov_b32 s27, 0
	v_add_u32_e32 v52, -1, v50
	v_cmp_lt_i32_e32 vcc, v52, v51
	s_mov_b64 s[10:11], -1
	v_mov_b32_e32 v228, s12
	v_cndmask_b32_e32 v52, v52, v50, vcc
	v_lshlrev_b32_e32 v203, 2, v52
	v_add_u32_e32 v52, -2, v50
	v_cmp_lt_i32_e32 vcc, v52, v51
	s_movk_i32 s28, 0x100
	s_movk_i32 s29, 0x80
	v_cndmask_b32_e32 v52, v52, v50, vcc
	v_lshlrev_b32_e32 v204, 2, v52
	v_add_u32_e32 v52, -4, v50
	v_cmp_lt_i32_e32 vcc, v52, v51
	s_movk_i32 s30, 0x220
	s_mov_b32 s31, 0x5040100
	v_cndmask_b32_e32 v52, v52, v50, vcc
	v_lshlrev_b32_e32 v205, 2, v52
	v_add_u32_e32 v52, -8, v50
	v_cmp_lt_i32_e32 vcc, v52, v51
	s_mov_b32 s33, 0x7060302
	v_mov_b32_e32 v209, 0x20000
	v_cndmask_b32_e32 v52, v52, v50, vcc
	v_lshlrev_b32_e32 v206, 2, v52
	v_add_u32_e32 v52, -16, v50
	v_cmp_lt_i32_e32 vcc, v52, v51
	v_mov_b32_e32 v219, 0x10000
	v_mov_b32_e32 v221, 0x80000
	v_cndmask_b32_e32 v52, v52, v50, vcc
	v_lshlrev_b32_e32 v207, 2, v52
	v_subrev_u32_e32 v52, 32, v50
	v_cmp_lt_i32_e32 vcc, v52, v51
	v_mov_b32_e32 v222, 0x100000
	v_mov_b32_e32 v223, 0x200000
	v_cndmask_b32_e32 v50, v52, v50, vcc
	v_lshlrev_b32_e32 v208, 2, v50
	v_mov_b32_e32 v224, 0x400000
	v_mov_b32_e32 v225, 0x800000
	v_mov_b32_e32 v226, 0x1000000
	v_bfrev_b32_e32 v227, 64
	v_bfrev_b32_e32 v229, 32
	v_bfrev_b32_e32 v230, 16
	v_bfrev_b32_e32 v231, 8
	v_bfrev_b32_e32 v232, 4
	v_bfrev_b32_e32 v233, 1
	s_waitcnt lgkmcnt(0)
	s_barrier
	s_branch .LBB1_84

.LBB1_116:
	s_or_b64 exec, exec, s[14:15]
	v_mov_b32_e32 v50, v0
	s_lshr_b32 s0, s34, 13
	v_and_b32_e32 v52, 15, v50
	s_waitcnt lgkmcnt(0)
	v_lshlrev_b32_e32 v55, 2, v50
	v_lshlrev_b32_e32 v52, 6, v52
	v_and_b32_e32 v53, 48, v50
	v_lshlrev_b32_e32 v54, 6, v50
	v_and_b32_e32 v55, 32, v55
	v_bitop3_b32 v237, v52, v55, v53 bitop3:0x36
	v_and_b32_e32 v52, 0x3c0, v54
	v_lshlrev_b32_e32 v56, 7, v50
	v_bitop3_b32 v52, v52, v55, v53 bitop3:0x36
	v_and_or_b32 v238, v56, s23, v52
	v_lshlrev_b32_e32 v52, 8, v50
	v_lshlrev_b32_e32 v53, 3, v50
	v_lshlrev_b32_e32 v50, 4, v50
	v_and_b32_e32 v52, 0x400, v52
	v_and_b32_e32 v55, 0x1c0, v53
	v_and_b32_e32 v50, 48, v50
	s_and_b32 s0, s0, 0x3800
	v_or3_b32 v50, v52, v50, v55
	v_and_b32_e32 v52, 0xfffff000, v54
	s_bfe_u32 s17, s34, 0x80010
	s_mulk_i32 s0, 0xc00
	v_or_b32_e32 v239, v50, v52
	v_bitop3_b32 v240, v50, s30, v52 bitop3:0x36
	v_and_or_b32 v50, v53, s26, v52
	s_add_u32 s0, s4, s0
	v_add_u32_e32 v241, 0x8000, v50
	v_add_u32_e32 v50, 0x8200, v50
	s_addc_u32 s1, s5, 0
	s_lshl_b32 s35, s17, 7
	v_xor_b32_e32 v242, 32, v50
	s_cmp_lt_u32 s34, 0x8000000
	v_mov_b32_e32 v50, 0x24000
	v_mov_b32_e32 v170, 0
	v_and_b32_e32 v236, 0x4000, v54
	v_lshl_add_u32 v243, v51, 10, v50
	s_cselect_b32 s1, s1, s7
	s_cselect_b32 s0, s0, s6
	s_mov_b32 s36, 0
	s_xor_b64 s[2:3], s[12:13], -1
	v_mov_b32_e32 v234, v228
	s_mov_b32 s16, s21
	s_mov_b32 s37, 0
	v_mov_b32_e32 v171, v170
	v_mov_b32_e32 v172, v170
	v_mov_b32_e32 v173, v170
	v_mov_b32_e32 v162, v170
	v_mov_b32_e32 v163, v170
	v_mov_b32_e32 v164, v170
	v_mov_b32_e32 v165, v170
	v_mov_b32_e32 v174, v170
	v_mov_b32_e32 v175, v170
	v_mov_b32_e32 v176, v170
	v_mov_b32_e32 v177, v170
	v_mov_b32_e32 v166, v170
	v_mov_b32_e32 v167, v170
	v_mov_b32_e32 v168, v170
	v_mov_b32_e32 v169, v170
	v_mov_b32_e32 v154, v170
	v_mov_b32_e32 v155, v170
	v_mov_b32_e32 v156, v170
	v_mov_b32_e32 v157, v170
	v_mov_b32_e32 v146, v170
	v_mov_b32_e32 v147, v170
	v_mov_b32_e32 v148, v170
	v_mov_b32_e32 v149, v170
	v_mov_b32_e32 v158, v170
	v_mov_b32_e32 v159, v170
	v_mov_b32_e32 v160, v170
	v_mov_b32_e32 v161, v170
	v_mov_b32_e32 v150, v170
	v_mov_b32_e32 v151, v170
	v_mov_b32_e32 v152, v170
	v_mov_b32_e32 v153, v170
	v_mov_b32_e32 v138, v170
	v_mov_b32_e32 v139, v170
	v_mov_b32_e32 v140, v170
	v_mov_b32_e32 v141, v170
	v_mov_b32_e32 v130, v170
	v_mov_b32_e32 v131, v170
	v_mov_b32_e32 v132, v170
	v_mov_b32_e32 v133, v170
	v_mov_b32_e32 v142, v170
	v_mov_b32_e32 v143, v170
	v_mov_b32_e32 v144, v170
	v_mov_b32_e32 v145, v170
	v_mov_b32_e32 v134, v170
	v_mov_b32_e32 v135, v170
	v_mov_b32_e32 v136, v170
	v_mov_b32_e32 v137, v170
	v_mov_b32_e32 v122, v170
	v_mov_b32_e32 v123, v170
	v_mov_b32_e32 v124, v170
	v_mov_b32_e32 v125, v170
	v_mov_b32_e32 v114, v170
	v_mov_b32_e32 v115, v170
	v_mov_b32_e32 v116, v170
	v_mov_b32_e32 v117, v170
	v_mov_b32_e32 v126, v170
	v_mov_b32_e32 v127, v170
	v_mov_b32_e32 v128, v170
	v_mov_b32_e32 v129, v170
	v_mov_b32_e32 v118, v170
	v_mov_b32_e32 v119, v170
	v_mov_b32_e32 v120, v170
	v_mov_b32_e32 v121, v170
	v_mov_b32_e32 v106, v170
	v_mov_b32_e32 v107, v170
	v_mov_b32_e32 v108, v170
	v_mov_b32_e32 v109, v170
	v_mov_b32_e32 v98, v170
	v_mov_b32_e32 v99, v170
	v_mov_b32_e32 v100, v170
	v_mov_b32_e32 v101, v170
	v_mov_b32_e32 v110, v170
	v_mov_b32_e32 v111, v170
	v_mov_b32_e32 v112, v170
	v_mov_b32_e32 v113, v170
	v_mov_b32_e32 v102, v170
	v_mov_b32_e32 v103, v170
	v_mov_b32_e32 v104, v170
	v_mov_b32_e32 v105, v170
	v_mov_b32_e32 v90, v170
	v_mov_b32_e32 v91, v170
	v_mov_b32_e32 v92, v170
	v_mov_b32_e32 v93, v170
	v_mov_b32_e32 v82, v170
	v_mov_b32_e32 v83, v170
	v_mov_b32_e32 v84, v170
	v_mov_b32_e32 v85, v170
	v_mov_b32_e32 v94, v170
	v_mov_b32_e32 v95, v170
	v_mov_b32_e32 v96, v170
	v_mov_b32_e32 v97, v170
	v_mov_b32_e32 v86, v170
	v_mov_b32_e32 v87, v170
	v_mov_b32_e32 v88, v170
	v_mov_b32_e32 v89, v170
	v_mov_b32_e32 v74, v170
	v_mov_b32_e32 v75, v170
	v_mov_b32_e32 v76, v170
	v_mov_b32_e32 v77, v170
	v_mov_b32_e32 v66, v170
	v_mov_b32_e32 v67, v170
	v_mov_b32_e32 v68, v170
	v_mov_b32_e32 v69, v170
	v_mov_b32_e32 v78, v170
	v_mov_b32_e32 v79, v170
	v_mov_b32_e32 v80, v170
	v_mov_b32_e32 v81, v170
	v_mov_b32_e32 v70, v170
	v_mov_b32_e32 v71, v170
	v_mov_b32_e32 v72, v170
	v_mov_b32_e32 v73, v170
	v_mov_b32_e32 v62, v170
	v_mov_b32_e32 v63, v170
	v_mov_b32_e32 v64, v170
	v_mov_b32_e32 v65, v170
	v_mov_b32_e32 v54, v170
	v_mov_b32_e32 v55, v170
	v_mov_b32_e32 v56, v170
	v_mov_b32_e32 v57, v170
	v_mov_b32_e32 v58, v170
	v_mov_b32_e32 v59, v170
	v_mov_b32_e32 v60, v170
	v_mov_b32_e32 v61, v170
	v_mov_b32_e32 v50, v170
	v_mov_b32_e32 v51, v170
	v_mov_b32_e32 v52, v170
	v_mov_b32_e32 v53, v170
	s_branch .LBB1_118
	s_nop 0
	s_nop 0
	s_nop 0
	s_nop 0
	s_nop 0
